# v50 + lever 7.3 on the SwiGLU epilogues (P6/P14): row pairs r, r+16 stored as one 16-B store per lane via v_permlane16_swap
# speedup vs baseline: 1.0119x; 1.0046x over previous
.LBB0_595:
	v_mbcnt_lo_u32_b32 v250, -1, 0
	v_mbcnt_hi_u32_b32 v250, -1, v250
	v_bfe_u32 v250, v250, 4, 1
	v_cmp_eq_u32_e32 vcc, 1, v250
	v_mov_b32_e32 v251, 0xffffc000
	v_mov_b32_e32 v250, -8
	s_nop 0
	v_cndmask_b32_e32 v250, v251, v250, vcc
	v_mov_b32_e32 v251, -1
	s_lshl_b32 s4, s84, 7
	v_mov_b32_e32 v17, v173
	v_mov_b32_e32 v0, v196
	s_or_b32 s4, s4, s69
	s_and_b64 vcc, exec, s[2:3]
	v_lshl_add_u32 v16, v0, 3, s4
	s_lshl_b32 s4, s85, 10
	s_and_b32 s4, s4, 0x400
	s_add_i32 s4, s70, s4
	v_lshl_add_u32 v0, v0, 5, s4
	ds_read_b128 v[12:15], v0
	ds_read_b128 v[4:7], v0 offset:16
	ds_read_b128 v[8:11], v0 offset:512
	ds_read_b128 v[0:3], v0 offset:528
	s_lshl_b32 s4, s83, 8
	s_waitcnt lgkmcnt(0)
	v_pk_fma_f32 v[20:21], v[156:157], s[22:23], v[12:13] op_sel_hi:[1,0,1]
	v_pk_fma_f32 v[26:27], v[158:159], s[22:23], v[14:15] op_sel_hi:[1,0,1]
	v_min_f32_e32 v20, 0x40e00000, v20
	v_min_f32_e32 v21, 0x40e00000, v21
	v_pk_mul_f32 v[22:23], v[20:21], s[24:25] op_sel_hi:[1,0]
	v_min_f32_e32 v26, 0x40e00000, v26
	v_exp_f32_e32 v22, v22
	v_exp_f32_e32 v23, v23
	v_min_f32_e32 v27, 0x40e00000, v27
	v_pk_mul_f32 v[28:29], v[26:27], s[24:25] op_sel_hi:[1,0]
	v_pk_fma_f32 v[24:25], v[152:153], s[22:23], v[8:9] op_sel_hi:[1,0,1]
	v_pk_add_f32 v[22:23], v[22:23], 1.0 op_sel_hi:[1,0]
	v_exp_f32_e32 v28, v28
	v_rcp_f32_e32 v22, v22
	v_rcp_f32_e32 v23, v23
	v_exp_f32_e32 v29, v29
	v_med3_f32 v24, v24, s78, v204
	v_med3_f32 v25, v25, s78, v204
	v_pk_mul_f32 v[20:21], v[20:21], v[22:23]
	v_pk_fma_f32 v[22:23], v[24:25], 4.0, 4.0 op_sel_hi:[1,0,0]
	v_pk_fma_f32 v[24:25], v[154:155], s[22:23], v[10:11] op_sel_hi:[1,0,1]
	v_pk_mul_f32 v[20:21], v[22:23], v[20:21]
	v_pk_add_f32 v[22:23], v[28:29], 1.0 op_sel_hi:[1,0]
	v_med3_f32 v24, v24, s78, v204
	v_rcp_f32_e32 v22, v22
	v_rcp_f32_e32 v23, v23
	v_med3_f32 v25, v25, s78, v204
	v_pk_fma_f32 v[24:25], v[24:25], 4.0, 4.0 op_sel_hi:[1,0,0]
	v_pk_fma_f32 v[30:31], v[150:151], s[22:23], v[6:7] op_sel_hi:[1,0,1]
	v_pk_mul_f32 v[22:23], v[26:27], v[22:23]
	v_min_f32_e32 v30, 0x40e00000, v30
	v_pk_mul_f32 v[22:23], v[24:25], v[22:23]
	v_pk_fma_f32 v[24:25], v[148:149], s[22:23], v[4:5] op_sel_hi:[1,0,1]
	v_min_f32_e32 v31, 0x40e00000, v31
	v_min_f32_e32 v24, 0x40e00000, v24
	v_min_f32_e32 v25, 0x40e00000, v25
	v_pk_mul_f32 v[26:27], v[24:25], s[24:25] op_sel_hi:[1,0]
	v_pk_fma_f32 v[28:29], v[144:145], s[22:23], v[0:1] op_sel_hi:[1,0,1]
	v_exp_f32_e32 v26, v26
	v_exp_f32_e32 v27, v27
	v_pk_mul_f32 v[144:145], v[30:31], s[24:25] op_sel_hi:[1,0]
	v_med3_f32 v28, v28, s78, v204
	v_exp_f32_e32 v144, v144
	v_pk_add_f32 v[26:27], v[26:27], 1.0 op_sel_hi:[1,0]
	v_exp_f32_e32 v145, v145
	v_rcp_f32_e32 v26, v26
	v_rcp_f32_e32 v27, v27
	v_med3_f32 v29, v29, s78, v204
	s_add_i32 s4, s4, s71
	v_add_u32_e32 v18, s4, v17
	v_pk_mul_f32 v[24:25], v[24:25], v[26:27]
	v_pk_fma_f32 v[26:27], v[28:29], 4.0, 4.0 op_sel_hi:[1,0,0]
	v_pk_fma_f32 v[28:29], v[146:147], s[22:23], v[2:3] op_sel_hi:[1,0,1]
	v_pk_mul_f32 v[24:25], v[26:27], v[24:25]
	v_pk_add_f32 v[26:27], v[144:145], 1.0 op_sel_hi:[1,0]
	v_med3_f32 v28, v28, s78, v204
	v_rcp_f32_e32 v26, v26
	v_rcp_f32_e32 v27, v27
	v_med3_f32 v29, v29, s78, v204
	v_ashrrev_i32_e32 v19, 31, v18
	v_ashrrev_i32_e32 v17, 31, v16
	v_pk_mul_f32 v[26:27], v[30:31], v[26:27]
	v_mov_b32_e32 v244, v165
	v_mov_b32_e32 v245, v165
	v_cvt_pk_fp8_f32 v244, v20, v21
	v_cvt_pk_fp8_f32 v245, v24, v25
	v_pk_fma_f32 v[20:21], v[28:29], 4.0, 4.0 op_sel_hi:[1,0,0]
	v_pk_fma_f32 v[24:25], v[136:137], s[22:23], v[8:9] op_sel_hi:[1,0,1]
	v_pk_mul_f32 v[20:21], v[20:21], v[26:27]
	v_cvt_pk_fp8_f32 v244, v22, v23 op_sel:[0,0,1]
	v_cvt_pk_fp8_f32 v245, v20, v21 op_sel:[0,0,1]
	v_lshlrev_b64 v[20:21], 10, v[18:19]
	v_lshl_add_u64 v[20:21], s[14:15], 0, v[20:21]
	v_lshl_add_u64 v[20:21], v[20:21], 0, v[16:17]
	v_pk_fma_f32 v[20:21], v[140:141], s[22:23], v[12:13] op_sel_hi:[1,0,1]
	v_pk_fma_f32 v[26:27], v[142:143], s[22:23], v[14:15] op_sel_hi:[1,0,1]
	v_min_f32_e32 v20, 0x40e00000, v20
	v_min_f32_e32 v21, 0x40e00000, v21
	v_pk_mul_f32 v[22:23], v[20:21], s[24:25] op_sel_hi:[1,0]
	v_min_f32_e32 v26, 0x40e00000, v26
	v_exp_f32_e32 v22, v22
	v_exp_f32_e32 v23, v23
	v_min_f32_e32 v27, 0x40e00000, v27
	v_pk_mul_f32 v[28:29], v[26:27], s[24:25] op_sel_hi:[1,0]
	v_med3_f32 v24, v24, s78, v204
	v_pk_add_f32 v[22:23], v[22:23], 1.0 op_sel_hi:[1,0]
	v_exp_f32_e32 v28, v28
	v_rcp_f32_e32 v22, v22
	v_rcp_f32_e32 v23, v23
	v_exp_f32_e32 v29, v29
	v_med3_f32 v25, v25, s78, v204
	v_pk_fma_f32 v[30:31], v[134:135], s[22:23], v[6:7] op_sel_hi:[1,0,1]
	v_pk_mul_f32 v[20:21], v[20:21], v[22:23]
	v_pk_fma_f32 v[22:23], v[24:25], 4.0, 4.0 op_sel_hi:[1,0,0]
	v_pk_fma_f32 v[24:25], v[138:139], s[22:23], v[10:11] op_sel_hi:[1,0,1]
	v_pk_mul_f32 v[20:21], v[22:23], v[20:21]
	v_pk_add_f32 v[22:23], v[28:29], 1.0 op_sel_hi:[1,0]
	v_med3_f32 v24, v24, s78, v204
	v_rcp_f32_e32 v22, v22
	v_rcp_f32_e32 v23, v23
	v_med3_f32 v25, v25, s78, v204
	v_pk_fma_f32 v[24:25], v[24:25], 4.0, 4.0 op_sel_hi:[1,0,0]
	v_min_f32_e32 v30, 0x40e00000, v30
	v_pk_mul_f32 v[22:23], v[26:27], v[22:23]
	v_min_f32_e32 v31, 0x40e00000, v31
	v_pk_mul_f32 v[22:23], v[24:25], v[22:23]
	v_pk_fma_f32 v[24:25], v[132:133], s[22:23], v[4:5] op_sel_hi:[1,0,1]
	v_pk_fma_f32 v[28:29], v[128:129], s[22:23], v[0:1] op_sel_hi:[1,0,1]
	v_min_f32_e32 v24, 0x40e00000, v24
	v_min_f32_e32 v25, 0x40e00000, v25
	v_pk_mul_f32 v[26:27], v[24:25], s[24:25] op_sel_hi:[1,0]
	v_pk_mul_f32 v[128:129], v[30:31], s[24:25] op_sel_hi:[1,0]
	v_exp_f32_e32 v26, v26
	v_exp_f32_e32 v27, v27
	v_exp_f32_e32 v128, v128
	v_exp_f32_e32 v129, v129
	v_med3_f32 v28, v28, s78, v204
	v_pk_add_f32 v[26:27], v[26:27], 1.0 op_sel_hi:[1,0]
	v_med3_f32 v29, v29, s78, v204
	v_rcp_f32_e32 v26, v26
	v_rcp_f32_e32 v27, v27
	s_mov_b64 s[2:3], -1
	v_pk_mul_f32 v[24:25], v[24:25], v[26:27]
	v_pk_fma_f32 v[26:27], v[28:29], 4.0, 4.0 op_sel_hi:[1,0,0]
	v_pk_fma_f32 v[28:29], v[130:131], s[22:23], v[2:3] op_sel_hi:[1,0,1]
	v_pk_mul_f32 v[24:25], v[26:27], v[24:25]
	v_pk_add_f32 v[26:27], v[128:129], 1.0 op_sel_hi:[1,0]
	v_med3_f32 v28, v28, s78, v204
	v_rcp_f32_e32 v26, v26
	v_rcp_f32_e32 v27, v27
	v_med3_f32 v29, v29, s78, v204
	v_pk_mul_f32 v[26:27], v[30:31], v[26:27]
	v_mov_b32_e32 v247, v165
	v_mov_b32_e32 v246, v165
	v_cvt_pk_fp8_f32 v247, v24, v25
	v_cvt_pk_fp8_f32 v246, v20, v21
	v_pk_fma_f32 v[20:21], v[28:29], 4.0, 4.0 op_sel_hi:[1,0,0]
	v_pk_fma_f32 v[24:25], v[120:121], s[22:23], v[8:9] op_sel_hi:[1,0,1]
	v_pk_mul_f32 v[20:21], v[20:21], v[26:27]
	v_cvt_pk_fp8_f32 v246, v22, v23 op_sel:[0,0,1]
	v_cvt_pk_fp8_f32 v247, v20, v21 op_sel:[0,0,1]
	v_add_u32_e32 v20, 16, v18
	v_ashrrev_i32_e32 v21, 31, v20
	v_lshlrev_b64 v[20:21], 10, v[20:21]
	v_lshl_add_u64 v[20:21], s[14:15], 0, v[20:21]
	v_lshl_add_u64 v[20:21], v[20:21], 0, v[16:17]
	s_nop 1
	v_permlane16_swap_b32_e32 v244, v246
	v_permlane16_swap_b32_e32 v245, v247
	v_lshl_add_u64 v[248:249], v[20:21], 0, v[250:251]
	global_store_dwordx4 v[248:249], v[244:247], off
	s_nop 1
	v_pk_fma_f32 v[20:21], v[124:125], s[22:23], v[12:13] op_sel_hi:[1,0,1]
	v_pk_fma_f32 v[26:27], v[126:127], s[22:23], v[14:15] op_sel_hi:[1,0,1]
	v_min_f32_e32 v20, 0x40e00000, v20
	v_min_f32_e32 v21, 0x40e00000, v21
	v_pk_mul_f32 v[22:23], v[20:21], s[24:25] op_sel_hi:[1,0]
	v_min_f32_e32 v26, 0x40e00000, v26
	v_exp_f32_e32 v22, v22
	v_exp_f32_e32 v23, v23
	v_min_f32_e32 v27, 0x40e00000, v27
	v_pk_mul_f32 v[28:29], v[26:27], s[24:25] op_sel_hi:[1,0]
	v_med3_f32 v24, v24, s78, v204
	v_pk_add_f32 v[22:23], v[22:23], 1.0 op_sel_hi:[1,0]
	v_exp_f32_e32 v28, v28
	v_rcp_f32_e32 v22, v22
	v_rcp_f32_e32 v23, v23
	v_exp_f32_e32 v29, v29
	v_med3_f32 v25, v25, s78, v204
	v_pk_fma_f32 v[30:31], v[118:119], s[22:23], v[6:7] op_sel_hi:[1,0,1]
	v_pk_mul_f32 v[20:21], v[20:21], v[22:23]
	v_pk_fma_f32 v[22:23], v[24:25], 4.0, 4.0 op_sel_hi:[1,0,0]
	v_pk_fma_f32 v[24:25], v[122:123], s[22:23], v[10:11] op_sel_hi:[1,0,1]
	v_pk_mul_f32 v[20:21], v[22:23], v[20:21]
	v_pk_add_f32 v[22:23], v[28:29], 1.0 op_sel_hi:[1,0]
	v_med3_f32 v24, v24, s78, v204
	v_rcp_f32_e32 v22, v22
	v_rcp_f32_e32 v23, v23
	v_med3_f32 v25, v25, s78, v204
	v_pk_fma_f32 v[24:25], v[24:25], 4.0, 4.0 op_sel_hi:[1,0,0]
	v_min_f32_e32 v30, 0x40e00000, v30
	v_pk_mul_f32 v[22:23], v[26:27], v[22:23]
	v_min_f32_e32 v31, 0x40e00000, v31
	v_pk_mul_f32 v[22:23], v[24:25], v[22:23]
	v_pk_fma_f32 v[24:25], v[116:117], s[22:23], v[4:5] op_sel_hi:[1,0,1]
	v_pk_fma_f32 v[28:29], v[112:113], s[22:23], v[0:1] op_sel_hi:[1,0,1]
	v_min_f32_e32 v24, 0x40e00000, v24
	v_min_f32_e32 v25, 0x40e00000, v25
	v_pk_mul_f32 v[26:27], v[24:25], s[24:25] op_sel_hi:[1,0]
	v_pk_mul_f32 v[112:113], v[30:31], s[24:25] op_sel_hi:[1,0]
	v_exp_f32_e32 v26, v26
	v_exp_f32_e32 v27, v27
	v_exp_f32_e32 v112, v112
	v_exp_f32_e32 v113, v113
	v_med3_f32 v28, v28, s78, v204
	v_pk_add_f32 v[26:27], v[26:27], 1.0 op_sel_hi:[1,0]
	v_med3_f32 v29, v29, s78, v204
	v_rcp_f32_e32 v26, v26
	v_rcp_f32_e32 v27, v27
	s_nop 0
	v_pk_mul_f32 v[24:25], v[24:25], v[26:27]
	v_pk_fma_f32 v[26:27], v[28:29], 4.0, 4.0 op_sel_hi:[1,0,0]
	v_pk_fma_f32 v[28:29], v[114:115], s[22:23], v[2:3] op_sel_hi:[1,0,1]
	v_pk_mul_f32 v[24:25], v[26:27], v[24:25]
	v_pk_add_f32 v[26:27], v[112:113], 1.0 op_sel_hi:[1,0]
	v_med3_f32 v28, v28, s78, v204
	v_rcp_f32_e32 v26, v26
	v_rcp_f32_e32 v27, v27
	v_med3_f32 v29, v29, s78, v204
	v_pk_mul_f32 v[26:27], v[30:31], v[26:27]
	v_mov_b32_e32 v245, v165
	v_mov_b32_e32 v244, v165
	v_cvt_pk_fp8_f32 v245, v24, v25
	v_cvt_pk_fp8_f32 v244, v20, v21
	v_pk_fma_f32 v[20:21], v[28:29], 4.0, 4.0 op_sel_hi:[1,0,0]
	v_pk_fma_f32 v[24:25], v[104:105], s[22:23], v[8:9] op_sel_hi:[1,0,1]
	v_pk_mul_f32 v[20:21], v[20:21], v[26:27]
	v_cvt_pk_fp8_f32 v244, v22, v23 op_sel:[0,0,1]
	v_cvt_pk_fp8_f32 v245, v20, v21 op_sel:[0,0,1]
	v_add_u32_e32 v20, 32, v18
	v_ashrrev_i32_e32 v21, 31, v20
	v_lshlrev_b64 v[20:21], 10, v[20:21]
	v_lshl_add_u64 v[20:21], s[14:15], 0, v[20:21]
	v_lshl_add_u64 v[20:21], v[20:21], 0, v[16:17]
	v_pk_fma_f32 v[20:21], v[108:109], s[22:23], v[12:13] op_sel_hi:[1,0,1]
	v_pk_fma_f32 v[26:27], v[110:111], s[22:23], v[14:15] op_sel_hi:[1,0,1]
	v_min_f32_e32 v20, 0x40e00000, v20
	v_min_f32_e32 v21, 0x40e00000, v21
	v_pk_mul_f32 v[22:23], v[20:21], s[24:25] op_sel_hi:[1,0]
	v_min_f32_e32 v26, 0x40e00000, v26
	v_exp_f32_e32 v22, v22
	v_exp_f32_e32 v23, v23
	v_min_f32_e32 v27, 0x40e00000, v27
	v_pk_mul_f32 v[28:29], v[26:27], s[24:25] op_sel_hi:[1,0]
	v_med3_f32 v24, v24, s78, v204
	v_pk_add_f32 v[22:23], v[22:23], 1.0 op_sel_hi:[1,0]
	v_exp_f32_e32 v28, v28
	v_rcp_f32_e32 v22, v22
	v_rcp_f32_e32 v23, v23
	v_exp_f32_e32 v29, v29
	v_med3_f32 v25, v25, s78, v204
	v_pk_fma_f32 v[30:31], v[102:103], s[22:23], v[6:7] op_sel_hi:[1,0,1]
	v_pk_mul_f32 v[20:21], v[20:21], v[22:23]
	v_pk_fma_f32 v[22:23], v[24:25], 4.0, 4.0 op_sel_hi:[1,0,0]
	v_pk_fma_f32 v[24:25], v[106:107], s[22:23], v[10:11] op_sel_hi:[1,0,1]
	v_pk_mul_f32 v[20:21], v[22:23], v[20:21]
	v_pk_add_f32 v[22:23], v[28:29], 1.0 op_sel_hi:[1,0]
	v_med3_f32 v24, v24, s78, v204
	v_rcp_f32_e32 v22, v22
	v_rcp_f32_e32 v23, v23
	v_med3_f32 v25, v25, s78, v204
	v_pk_fma_f32 v[24:25], v[24:25], 4.0, 4.0 op_sel_hi:[1,0,0]
	v_min_f32_e32 v30, 0x40e00000, v30
	v_pk_mul_f32 v[22:23], v[26:27], v[22:23]
	v_min_f32_e32 v31, 0x40e00000, v31
	v_pk_mul_f32 v[22:23], v[24:25], v[22:23]
	v_pk_fma_f32 v[24:25], v[100:101], s[22:23], v[4:5] op_sel_hi:[1,0,1]
	v_pk_fma_f32 v[28:29], v[96:97], s[22:23], v[0:1] op_sel_hi:[1,0,1]
	v_min_f32_e32 v24, 0x40e00000, v24
	v_min_f32_e32 v25, 0x40e00000, v25
	v_pk_mul_f32 v[26:27], v[24:25], s[24:25] op_sel_hi:[1,0]
	v_pk_mul_f32 v[96:97], v[30:31], s[24:25] op_sel_hi:[1,0]
	v_exp_f32_e32 v26, v26
	v_exp_f32_e32 v27, v27
	v_exp_f32_e32 v96, v96
	v_exp_f32_e32 v97, v97
	v_med3_f32 v28, v28, s78, v204
	v_pk_add_f32 v[26:27], v[26:27], 1.0 op_sel_hi:[1,0]
	v_med3_f32 v29, v29, s78, v204
	v_rcp_f32_e32 v26, v26
	v_rcp_f32_e32 v27, v27
	s_nop 0
	v_pk_mul_f32 v[24:25], v[24:25], v[26:27]
	v_pk_fma_f32 v[26:27], v[28:29], 4.0, 4.0 op_sel_hi:[1,0,0]
	v_pk_fma_f32 v[28:29], v[98:99], s[22:23], v[2:3] op_sel_hi:[1,0,1]
	v_pk_mul_f32 v[24:25], v[26:27], v[24:25]
	v_pk_add_f32 v[26:27], v[96:97], 1.0 op_sel_hi:[1,0]
	v_med3_f32 v28, v28, s78, v204
	v_rcp_f32_e32 v26, v26
	v_rcp_f32_e32 v27, v27
	v_med3_f32 v29, v29, s78, v204
	v_pk_mul_f32 v[26:27], v[30:31], v[26:27]
	v_mov_b32_e32 v246, v165
	v_cvt_pk_fp8_f32 v246, v20, v21
	v_mov_b32_e32 v247, v165
	v_cvt_pk_fp8_f32 v247, v24, v25
	v_pk_fma_f32 v[20:21], v[28:29], 4.0, 4.0 op_sel_hi:[1,0,0]
	v_cvt_pk_fp8_f32 v246, v22, v23 op_sel:[0,0,1]
	v_pk_fma_f32 v[22:23], v[92:93], s[22:23], v[12:13] op_sel_hi:[1,0,1]
	v_pk_mul_f32 v[20:21], v[20:21], v[26:27]
	v_min_f32_e32 v22, 0x40e00000, v22
	v_min_f32_e32 v23, 0x40e00000, v23
	v_pk_mul_f32 v[24:25], v[22:23], s[24:25] op_sel_hi:[1,0]
	v_cvt_pk_fp8_f32 v247, v20, v21 op_sel:[0,0,1]
	v_add_u32_e32 v20, 48, v18
	v_exp_f32_e32 v24, v24
	v_exp_f32_e32 v25, v25
	v_ashrrev_i32_e32 v21, 31, v20
	v_lshlrev_b64 v[20:21], 10, v[20:21]
	v_lshl_add_u64 v[20:21], s[14:15], 0, v[20:21]
	v_pk_fma_f32 v[28:29], v[94:95], s[22:23], v[14:15] op_sel_hi:[1,0,1]
	v_lshl_add_u64 v[20:21], v[20:21], 0, v[16:17]
	v_pk_add_f32 v[24:25], v[24:25], 1.0 op_sel_hi:[1,0]
	v_min_f32_e32 v28, 0x40e00000, v28
	v_min_f32_e32 v29, 0x40e00000, v29
	s_nop 1
	v_permlane16_swap_b32_e32 v244, v246
	v_permlane16_swap_b32_e32 v245, v247
	v_lshl_add_u64 v[248:249], v[20:21], 0, v[250:251]
	global_store_dwordx4 v[248:249], v[244:247], off
	s_nop 1
	v_rcp_f32_e32 v24, v24
	v_rcp_f32_e32 v25, v25
	v_pk_mul_f32 v[30:31], v[28:29], s[24:25] op_sel_hi:[1,0]
	v_pk_fma_f32 v[26:27], v[88:89], s[22:23], v[8:9] op_sel_hi:[1,0,1]
	v_exp_f32_e32 v30, v30
	v_exp_f32_e32 v31, v31
	v_med3_f32 v26, v26, s78, v204
	v_med3_f32 v27, v27, s78, v204
	v_pk_mul_f32 v[22:23], v[22:23], v[24:25]
	v_pk_fma_f32 v[24:25], v[26:27], 4.0, 4.0 op_sel_hi:[1,0,0]
	v_pk_fma_f32 v[26:27], v[90:91], s[22:23], v[10:11] op_sel_hi:[1,0,1]
	v_pk_mul_f32 v[22:23], v[24:25], v[22:23]
	v_pk_add_f32 v[24:25], v[30:31], 1.0 op_sel_hi:[1,0]
	v_med3_f32 v26, v26, s78, v204
	v_rcp_f32_e32 v24, v24
	v_rcp_f32_e32 v25, v25
	v_med3_f32 v27, v27, s78, v204
	v_pk_fma_f32 v[26:27], v[26:27], 4.0, 4.0 op_sel_hi:[1,0,0]
	v_pk_fma_f32 v[30:31], v[80:81], s[22:23], v[0:1] op_sel_hi:[1,0,1]
	v_pk_mul_f32 v[24:25], v[28:29], v[24:25]
	v_pk_fma_f32 v[80:81], v[86:87], s[22:23], v[6:7] op_sel_hi:[1,0,1]
	v_pk_mul_f32 v[24:25], v[26:27], v[24:25]
	v_pk_fma_f32 v[26:27], v[84:85], s[22:23], v[4:5] op_sel_hi:[1,0,1]
	v_min_f32_e32 v80, 0x40e00000, v80
	v_min_f32_e32 v26, 0x40e00000, v26
	v_min_f32_e32 v27, 0x40e00000, v27
	v_pk_mul_f32 v[28:29], v[26:27], s[24:25] op_sel_hi:[1,0]
	v_min_f32_e32 v81, 0x40e00000, v81
	v_exp_f32_e32 v28, v28
	v_exp_f32_e32 v29, v29
	v_pk_mul_f32 v[84:85], v[80:81], s[24:25] op_sel_hi:[1,0]
	v_med3_f32 v30, v30, s78, v204
	v_exp_f32_e32 v84, v84
	v_pk_add_f32 v[28:29], v[28:29], 1.0 op_sel_hi:[1,0]
	v_exp_f32_e32 v85, v85
	v_rcp_f32_e32 v28, v28
	v_rcp_f32_e32 v29, v29
	v_med3_f32 v31, v31, s78, v204
	v_add_u32_e32 v20, 0x80, v18
	v_ashrrev_i32_e32 v21, 31, v20
	v_pk_mul_f32 v[26:27], v[26:27], v[28:29]
	v_pk_fma_f32 v[28:29], v[30:31], 4.0, 4.0 op_sel_hi:[1,0,0]
	v_pk_fma_f32 v[30:31], v[82:83], s[22:23], v[2:3] op_sel_hi:[1,0,1]
	v_pk_mul_f32 v[26:27], v[28:29], v[26:27]
	v_pk_add_f32 v[28:29], v[84:85], 1.0 op_sel_hi:[1,0]
	v_med3_f32 v30, v30, s78, v204
	v_rcp_f32_e32 v28, v28
	v_rcp_f32_e32 v29, v29
	v_med3_f32 v31, v31, s78, v204
	v_lshlrev_b64 v[20:21], 10, v[20:21]
	v_lshl_add_u64 v[20:21], s[14:15], 0, v[20:21]
	v_pk_mul_f32 v[28:29], v[80:81], v[28:29]
	v_mov_b32_e32 v244, v165
	v_mov_b32_e32 v245, v165
	v_cvt_pk_fp8_f32 v244, v22, v23
	v_cvt_pk_fp8_f32 v245, v26, v27
	v_pk_fma_f32 v[22:23], v[30:31], 4.0, 4.0 op_sel_hi:[1,0,0]
	v_lshl_add_u64 v[20:21], v[20:21], 0, v[16:17]
	v_pk_mul_f32 v[22:23], v[22:23], v[28:29]
	v_cvt_pk_fp8_f32 v244, v24, v25 op_sel:[0,0,1]
	v_cvt_pk_fp8_f32 v245, v22, v23 op_sel:[0,0,1]
	v_pk_fma_f32 v[26:27], v[78:79], s[22:23], v[14:15] op_sel_hi:[1,0,1]
	v_pk_fma_f32 v[24:25], v[72:73], s[22:23], v[8:9] op_sel_hi:[1,0,1]
	v_min_f32_e32 v26, 0x40e00000, v26
	v_pk_fma_f32 v[20:21], v[76:77], s[22:23], v[12:13] op_sel_hi:[1,0,1]
	v_min_f32_e32 v27, 0x40e00000, v27
	v_min_f32_e32 v20, 0x40e00000, v20
	v_min_f32_e32 v21, 0x40e00000, v21
	v_pk_mul_f32 v[22:23], v[20:21], s[24:25] op_sel_hi:[1,0]
	v_pk_mul_f32 v[28:29], v[26:27], s[24:25] op_sel_hi:[1,0]
	v_exp_f32_e32 v22, v22
	v_exp_f32_e32 v23, v23
	v_exp_f32_e32 v28, v28
	v_exp_f32_e32 v29, v29
	v_med3_f32 v24, v24, s78, v204
	v_pk_add_f32 v[22:23], v[22:23], 1.0 op_sel_hi:[1,0]
	v_med3_f32 v25, v25, s78, v204
	v_rcp_f32_e32 v22, v22
	v_rcp_f32_e32 v23, v23
	v_pk_fma_f32 v[30:31], v[70:71], s[22:23], v[6:7] op_sel_hi:[1,0,1]
	v_pk_mul_f32 v[20:21], v[20:21], v[22:23]
	v_pk_fma_f32 v[22:23], v[24:25], 4.0, 4.0 op_sel_hi:[1,0,0]
	v_pk_fma_f32 v[24:25], v[74:75], s[22:23], v[10:11] op_sel_hi:[1,0,1]
	v_pk_mul_f32 v[20:21], v[22:23], v[20:21]
	v_pk_add_f32 v[22:23], v[28:29], 1.0 op_sel_hi:[1,0]
	v_med3_f32 v24, v24, s78, v204
	v_rcp_f32_e32 v22, v22
	v_rcp_f32_e32 v23, v23
	v_med3_f32 v25, v25, s78, v204
	v_pk_fma_f32 v[24:25], v[24:25], 4.0, 4.0 op_sel_hi:[1,0,0]
	v_min_f32_e32 v30, 0x40e00000, v30
	v_pk_mul_f32 v[22:23], v[26:27], v[22:23]
	v_min_f32_e32 v31, 0x40e00000, v31
	v_pk_mul_f32 v[22:23], v[24:25], v[22:23]
	v_pk_fma_f32 v[24:25], v[68:69], s[22:23], v[4:5] op_sel_hi:[1,0,1]
	v_pk_fma_f32 v[28:29], v[64:65], s[22:23], v[0:1] op_sel_hi:[1,0,1]
	v_min_f32_e32 v24, 0x40e00000, v24
	v_min_f32_e32 v25, 0x40e00000, v25
	v_pk_mul_f32 v[26:27], v[24:25], s[24:25] op_sel_hi:[1,0]
	v_pk_mul_f32 v[64:65], v[30:31], s[24:25] op_sel_hi:[1,0]
	v_exp_f32_e32 v26, v26
	v_exp_f32_e32 v27, v27
	v_exp_f32_e32 v64, v64
	v_exp_f32_e32 v65, v65
	v_med3_f32 v28, v28, s78, v204
	v_pk_add_f32 v[26:27], v[26:27], 1.0 op_sel_hi:[1,0]
	v_med3_f32 v29, v29, s78, v204
	v_rcp_f32_e32 v26, v26
	v_rcp_f32_e32 v27, v27
	s_nop 0
	v_pk_mul_f32 v[24:25], v[24:25], v[26:27]
	v_pk_fma_f32 v[26:27], v[28:29], 4.0, 4.0 op_sel_hi:[1,0,0]
	v_pk_fma_f32 v[28:29], v[66:67], s[22:23], v[2:3] op_sel_hi:[1,0,1]
	v_pk_mul_f32 v[24:25], v[26:27], v[24:25]
	v_pk_add_f32 v[26:27], v[64:65], 1.0 op_sel_hi:[1,0]
	v_med3_f32 v28, v28, s78, v204
	v_rcp_f32_e32 v26, v26
	v_rcp_f32_e32 v27, v27
	v_med3_f32 v29, v29, s78, v204
	v_pk_mul_f32 v[26:27], v[30:31], v[26:27]
	v_mov_b32_e32 v247, v165
	v_mov_b32_e32 v246, v165
	v_cvt_pk_fp8_f32 v247, v24, v25
	v_cvt_pk_fp8_f32 v246, v20, v21
	v_pk_fma_f32 v[20:21], v[28:29], 4.0, 4.0 op_sel_hi:[1,0,0]
	v_pk_fma_f32 v[24:25], v[56:57], s[22:23], v[8:9] op_sel_hi:[1,0,1]
	v_pk_mul_f32 v[20:21], v[20:21], v[26:27]
	v_cvt_pk_fp8_f32 v246, v22, v23 op_sel:[0,0,1]
	v_cvt_pk_fp8_f32 v247, v20, v21 op_sel:[0,0,1]
	v_add_u32_e32 v20, 0x90, v18
	v_ashrrev_i32_e32 v21, 31, v20
	v_lshlrev_b64 v[20:21], 10, v[20:21]
	v_lshl_add_u64 v[20:21], s[14:15], 0, v[20:21]
	v_lshl_add_u64 v[20:21], v[20:21], 0, v[16:17]
	s_nop 1
	v_permlane16_swap_b32_e32 v244, v246
	v_permlane16_swap_b32_e32 v245, v247
	v_lshl_add_u64 v[248:249], v[20:21], 0, v[250:251]
	global_store_dwordx4 v[248:249], v[244:247], off
	s_nop 1
	v_pk_fma_f32 v[20:21], v[60:61], s[22:23], v[12:13] op_sel_hi:[1,0,1]
	v_pk_fma_f32 v[26:27], v[62:63], s[22:23], v[14:15] op_sel_hi:[1,0,1]
	v_min_f32_e32 v20, 0x40e00000, v20
	v_min_f32_e32 v21, 0x40e00000, v21
	v_pk_mul_f32 v[22:23], v[20:21], s[24:25] op_sel_hi:[1,0]
	v_min_f32_e32 v26, 0x40e00000, v26
	v_exp_f32_e32 v22, v22
	v_exp_f32_e32 v23, v23
	v_min_f32_e32 v27, 0x40e00000, v27
	v_pk_mul_f32 v[28:29], v[26:27], s[24:25] op_sel_hi:[1,0]
	v_med3_f32 v24, v24, s78, v204
	v_pk_add_f32 v[22:23], v[22:23], 1.0 op_sel_hi:[1,0]
	v_exp_f32_e32 v28, v28
	v_rcp_f32_e32 v22, v22
	v_rcp_f32_e32 v23, v23
	v_exp_f32_e32 v29, v29
	v_med3_f32 v25, v25, s78, v204
	v_pk_fma_f32 v[30:31], v[54:55], s[22:23], v[6:7] op_sel_hi:[1,0,1]
	v_pk_mul_f32 v[20:21], v[20:21], v[22:23]
	v_pk_fma_f32 v[22:23], v[24:25], 4.0, 4.0 op_sel_hi:[1,0,0]
	v_pk_fma_f32 v[24:25], v[58:59], s[22:23], v[10:11] op_sel_hi:[1,0,1]
	v_pk_mul_f32 v[20:21], v[22:23], v[20:21]
	v_pk_add_f32 v[22:23], v[28:29], 1.0 op_sel_hi:[1,0]
	v_med3_f32 v24, v24, s78, v204
	v_rcp_f32_e32 v22, v22
	v_rcp_f32_e32 v23, v23
	v_med3_f32 v25, v25, s78, v204
	v_pk_fma_f32 v[24:25], v[24:25], 4.0, 4.0 op_sel_hi:[1,0,0]
	v_min_f32_e32 v30, 0x40e00000, v30
	v_pk_mul_f32 v[22:23], v[26:27], v[22:23]
	v_min_f32_e32 v31, 0x40e00000, v31
	v_pk_mul_f32 v[22:23], v[24:25], v[22:23]
	v_pk_fma_f32 v[24:25], v[52:53], s[22:23], v[4:5] op_sel_hi:[1,0,1]
	v_pk_fma_f32 v[28:29], v[48:49], s[22:23], v[0:1] op_sel_hi:[1,0,1]
	v_min_f32_e32 v24, 0x40e00000, v24
	v_min_f32_e32 v25, 0x40e00000, v25
	v_pk_mul_f32 v[26:27], v[24:25], s[24:25] op_sel_hi:[1,0]
	v_pk_mul_f32 v[48:49], v[30:31], s[24:25] op_sel_hi:[1,0]
	v_exp_f32_e32 v26, v26
	v_exp_f32_e32 v27, v27
	v_exp_f32_e32 v48, v48
	v_exp_f32_e32 v49, v49
	v_med3_f32 v28, v28, s78, v204
	v_pk_add_f32 v[26:27], v[26:27], 1.0 op_sel_hi:[1,0]
	v_med3_f32 v29, v29, s78, v204
	v_rcp_f32_e32 v26, v26
	v_rcp_f32_e32 v27, v27
	v_pk_fma_f32 v[12:13], v[44:45], s[22:23], v[12:13] op_sel_hi:[1,0,1]
	v_pk_fma_f32 v[14:15], v[46:47], s[22:23], v[14:15] op_sel_hi:[1,0,1]
	v_min_f32_e32 v12, 0x40e00000, v12
	v_pk_mul_f32 v[24:25], v[24:25], v[26:27]
	v_pk_fma_f32 v[26:27], v[28:29], 4.0, 4.0 op_sel_hi:[1,0,0]
	v_pk_fma_f32 v[28:29], v[50:51], s[22:23], v[2:3] op_sel_hi:[1,0,1]
	v_pk_mul_f32 v[24:25], v[26:27], v[24:25]
	v_pk_add_f32 v[26:27], v[48:49], 1.0 op_sel_hi:[1,0]
	v_med3_f32 v28, v28, s78, v204
	v_rcp_f32_e32 v26, v26
	v_rcp_f32_e32 v27, v27
	v_med3_f32 v29, v29, s78, v204
	v_min_f32_e32 v13, 0x40e00000, v13
	v_min_f32_e32 v14, 0x40e00000, v14
	v_pk_mul_f32 v[26:27], v[30:31], v[26:27]
	v_mov_b32_e32 v245, v165
	v_mov_b32_e32 v244, v165
	v_cvt_pk_fp8_f32 v245, v24, v25
	v_cvt_pk_fp8_f32 v244, v20, v21
	v_pk_fma_f32 v[20:21], v[28:29], 4.0, 4.0 op_sel_hi:[1,0,0]
	v_min_f32_e32 v15, 0x40e00000, v15
	v_pk_mul_f32 v[20:21], v[20:21], v[26:27]
	v_cvt_pk_fp8_f32 v244, v22, v23 op_sel:[0,0,1]
	v_cvt_pk_fp8_f32 v245, v20, v21 op_sel:[0,0,1]
	v_add_u32_e32 v20, 0xa0, v18
	v_ashrrev_i32_e32 v21, 31, v20
	v_lshlrev_b64 v[20:21], 10, v[20:21]
	v_lshl_add_u64 v[20:21], s[14:15], 0, v[20:21]
	v_lshl_add_u64 v[20:21], v[20:21], 0, v[16:17]
	v_pk_mul_f32 v[20:21], v[12:13], s[24:25] op_sel_hi:[1,0]
	v_pk_mul_f32 v[22:23], v[14:15], s[24:25] op_sel_hi:[1,0]
	v_exp_f32_e32 v20, v20
	v_exp_f32_e32 v21, v21
	v_exp_f32_e32 v22, v22
	v_exp_f32_e32 v23, v23
	v_pk_fma_f32 v[8:9], v[40:41], s[22:23], v[8:9] op_sel_hi:[1,0,1]
	v_pk_add_f32 v[20:21], v[20:21], 1.0 op_sel_hi:[1,0]
	v_med3_f32 v8, v8, s78, v204
	v_rcp_f32_e32 v20, v20
	v_rcp_f32_e32 v21, v21
	v_med3_f32 v9, v9, s78, v204
	v_pk_fma_f32 v[8:9], v[8:9], 4.0, 4.0 op_sel_hi:[1,0,0]
	v_pk_fma_f32 v[10:11], v[42:43], s[22:23], v[10:11] op_sel_hi:[1,0,1]
	v_pk_mul_f32 v[12:13], v[12:13], v[20:21]
	v_med3_f32 v10, v10, s78, v204
	v_pk_mul_f32 v[8:9], v[8:9], v[12:13]
	v_pk_add_f32 v[12:13], v[22:23], 1.0 op_sel_hi:[1,0]
	v_med3_f32 v11, v11, s78, v204
	v_rcp_f32_e32 v12, v12
	v_rcp_f32_e32 v13, v13
	v_pk_fma_f32 v[4:5], v[36:37], s[22:23], v[4:5] op_sel_hi:[1,0,1]
	v_pk_fma_f32 v[10:11], v[10:11], 4.0, 4.0 op_sel_hi:[1,0,0]
	v_min_f32_e32 v4, 0x40e00000, v4
	v_pk_mul_f32 v[12:13], v[14:15], v[12:13]
	v_min_f32_e32 v5, 0x40e00000, v5
	v_pk_mul_f32 v[10:11], v[10:11], v[12:13]
	v_pk_mul_f32 v[12:13], v[4:5], s[24:25] op_sel_hi:[1,0]
	v_pk_fma_f32 v[6:7], v[38:39], s[22:23], v[6:7] op_sel_hi:[1,0,1]
	v_exp_f32_e32 v12, v12
	v_exp_f32_e32 v13, v13
	v_min_f32_e32 v6, 0x40e00000, v6
	v_min_f32_e32 v7, 0x40e00000, v7
	v_pk_mul_f32 v[14:15], v[6:7], s[24:25] op_sel_hi:[1,0]
	v_pk_add_f32 v[12:13], v[12:13], 1.0 op_sel_hi:[1,0]
	v_exp_f32_e32 v14, v14
	v_rcp_f32_e32 v12, v12
	v_rcp_f32_e32 v13, v13
	v_exp_f32_e32 v15, v15
	v_pk_fma_f32 v[0:1], v[32:33], s[22:23], v[0:1] op_sel_hi:[1,0,1]
	v_pk_fma_f32 v[2:3], v[34:35], s[22:23], v[2:3] op_sel_hi:[1,0,1]
	v_med3_f32 v0, v0, s78, v204
	v_med3_f32 v1, v1, s78, v204
	v_pk_mul_f32 v[4:5], v[4:5], v[12:13]
	v_pk_fma_f32 v[0:1], v[0:1], 4.0, 4.0 op_sel_hi:[1,0,0]
	v_med3_f32 v2, v2, s78, v204
	v_pk_mul_f32 v[0:1], v[0:1], v[4:5]
	v_pk_add_f32 v[4:5], v[14:15], 1.0 op_sel_hi:[1,0]
	v_med3_f32 v3, v3, s78, v204
	v_rcp_f32_e32 v4, v4
	v_rcp_f32_e32 v5, v5
	s_nop 0
	v_pk_mul_f32 v[4:5], v[6:7], v[4:5]
	v_mov_b32_e32 v247, v165
	v_mov_b32_e32 v246, v165
	v_cvt_pk_fp8_f32 v247, v0, v1
	v_cvt_pk_fp8_f32 v246, v8, v9
	v_pk_fma_f32 v[0:1], v[2:3], 4.0, 4.0 op_sel_hi:[1,0,0]
	v_cvt_pk_fp8_f32 v246, v10, v11 op_sel:[0,0,1]
	v_pk_mul_f32 v[0:1], v[0:1], v[4:5]
	s_nop 0
	v_cvt_pk_fp8_f32 v247, v0, v1 op_sel:[0,0,1]
	v_add_u32_e32 v0, 0xb0, v18
	v_ashrrev_i32_e32 v1, 31, v0
	v_lshlrev_b64 v[0:1], 10, v[0:1]
	v_lshl_add_u64 v[0:1], s[14:15], 0, v[0:1]
	v_lshl_add_u64 v[0:1], v[0:1], 0, v[16:17]
	s_nop 1
	v_permlane16_swap_b32_e32 v244, v246
	v_permlane16_swap_b32_e32 v245, v247
	v_lshl_add_u64 v[248:249], v[0:1], 0, v[250:251]
	global_store_dwordx4 v[248:249], v[244:247], off
	s_nop 1
	s_cbranch_vccnz .LBB0_581
	s_andn2_b64 vcc, exec, s[12:13]
	s_cbranch_vccnz .LBB0_580
	s_barrier
	s_branch .LBB0_580

.LBB0_1714:
	v_mbcnt_lo_u32_b32 v250, -1, 0
	v_mbcnt_hi_u32_b32 v250, -1, v250
	v_bfe_u32 v250, v250, 4, 1
	v_cmp_eq_u32_e32 vcc, 1, v250
	v_mov_b32_e32 v251, 0xffffc000
	v_mov_b32_e32 v250, -8
	s_nop 0
	v_cndmask_b32_e32 v250, v251, v250, vcc
	v_mov_b32_e32 v251, -1
	s_lshl_b32 s4, s84, 7
	v_mov_b32_e32 v0, v196
	v_mov_b32_e32 v17, v173
	s_or_b32 s4, s4, s69
	s_and_b64 vcc, exec, s[2:3]
	v_lshl_add_u32 v16, v0, 3, s4
	s_lshl_b32 s4, s85, 10
	s_and_b32 s4, s4, 0x400
	s_add_i32 s4, s70, s4
	v_lshl_add_u32 v0, v0, 5, s4
	ds_read_b128 v[12:15], v0
	ds_read_b128 v[4:7], v0 offset:16
	ds_read_b128 v[8:11], v0 offset:512
	ds_read_b128 v[0:3], v0 offset:528
	s_lshl_b32 s4, s83, 8
	s_waitcnt lgkmcnt(0)
	v_pk_fma_f32 v[20:21], v[156:157], s[22:23], v[12:13] op_sel_hi:[1,0,1]
	v_pk_fma_f32 v[26:27], v[158:159], s[22:23], v[14:15] op_sel_hi:[1,0,1]
	v_min_f32_e32 v20, 0x40e00000, v20
	v_min_f32_e32 v21, 0x40e00000, v21
	v_pk_mul_f32 v[22:23], v[20:21], s[24:25] op_sel_hi:[1,0]
	v_min_f32_e32 v26, 0x40e00000, v26
	v_exp_f32_e32 v22, v22
	v_exp_f32_e32 v23, v23
	v_min_f32_e32 v27, 0x40e00000, v27
	v_pk_mul_f32 v[28:29], v[26:27], s[24:25] op_sel_hi:[1,0]
	v_pk_fma_f32 v[24:25], v[152:153], s[22:23], v[8:9] op_sel_hi:[1,0,1]
	v_pk_add_f32 v[22:23], v[22:23], 1.0 op_sel_hi:[1,0]
	v_exp_f32_e32 v28, v28
	v_rcp_f32_e32 v22, v22
	v_rcp_f32_e32 v23, v23
	v_exp_f32_e32 v29, v29
	v_med3_f32 v24, v24, s78, v204
	v_med3_f32 v25, v25, s78, v204
	v_pk_mul_f32 v[20:21], v[20:21], v[22:23]
	v_pk_fma_f32 v[22:23], v[24:25], 4.0, 4.0 op_sel_hi:[1,0,0]
	v_pk_fma_f32 v[24:25], v[154:155], s[22:23], v[10:11] op_sel_hi:[1,0,1]
	v_pk_mul_f32 v[20:21], v[22:23], v[20:21]
	v_pk_add_f32 v[22:23], v[28:29], 1.0 op_sel_hi:[1,0]
	v_med3_f32 v24, v24, s78, v204
	v_rcp_f32_e32 v22, v22
	v_rcp_f32_e32 v23, v23
	v_med3_f32 v25, v25, s78, v204
	v_pk_fma_f32 v[24:25], v[24:25], 4.0, 4.0 op_sel_hi:[1,0,0]
	v_pk_fma_f32 v[30:31], v[150:151], s[22:23], v[6:7] op_sel_hi:[1,0,1]
	v_pk_mul_f32 v[22:23], v[26:27], v[22:23]
	v_min_f32_e32 v30, 0x40e00000, v30
	v_pk_mul_f32 v[22:23], v[24:25], v[22:23]
	v_pk_fma_f32 v[24:25], v[148:149], s[22:23], v[4:5] op_sel_hi:[1,0,1]
	v_min_f32_e32 v31, 0x40e00000, v31
	v_min_f32_e32 v24, 0x40e00000, v24
	v_min_f32_e32 v25, 0x40e00000, v25
	v_pk_mul_f32 v[26:27], v[24:25], s[24:25] op_sel_hi:[1,0]
	v_pk_fma_f32 v[28:29], v[144:145], s[22:23], v[0:1] op_sel_hi:[1,0,1]
	v_exp_f32_e32 v26, v26
	v_exp_f32_e32 v27, v27
	v_pk_mul_f32 v[144:145], v[30:31], s[24:25] op_sel_hi:[1,0]
	v_med3_f32 v28, v28, s78, v204
	v_exp_f32_e32 v144, v144
	v_pk_add_f32 v[26:27], v[26:27], 1.0 op_sel_hi:[1,0]
	v_exp_f32_e32 v145, v145
	v_rcp_f32_e32 v26, v26
	v_rcp_f32_e32 v27, v27
	v_med3_f32 v29, v29, s78, v204
	s_add_i32 s4, s4, s71
	v_add_u32_e32 v18, s4, v17
	v_pk_mul_f32 v[24:25], v[24:25], v[26:27]
	v_pk_fma_f32 v[26:27], v[28:29], 4.0, 4.0 op_sel_hi:[1,0,0]
	v_pk_fma_f32 v[28:29], v[146:147], s[22:23], v[2:3] op_sel_hi:[1,0,1]
	v_pk_mul_f32 v[24:25], v[26:27], v[24:25]
	v_pk_add_f32 v[26:27], v[144:145], 1.0 op_sel_hi:[1,0]
	v_med3_f32 v28, v28, s78, v204
	v_rcp_f32_e32 v26, v26
	v_rcp_f32_e32 v27, v27
	v_med3_f32 v29, v29, s78, v204
	v_ashrrev_i32_e32 v19, 31, v18
	v_ashrrev_i32_e32 v17, 31, v16
	v_pk_mul_f32 v[26:27], v[30:31], v[26:27]
	v_mov_b32_e32 v244, v165
	v_mov_b32_e32 v245, v165
	v_cvt_pk_fp8_f32 v244, v20, v21
	v_cvt_pk_fp8_f32 v245, v24, v25
	v_pk_fma_f32 v[20:21], v[28:29], 4.0, 4.0 op_sel_hi:[1,0,0]
	v_pk_fma_f32 v[24:25], v[136:137], s[22:23], v[8:9] op_sel_hi:[1,0,1]
	v_pk_mul_f32 v[20:21], v[20:21], v[26:27]
	v_cvt_pk_fp8_f32 v244, v22, v23 op_sel:[0,0,1]
	v_cvt_pk_fp8_f32 v245, v20, v21 op_sel:[0,0,1]
	v_lshlrev_b64 v[20:21], 10, v[18:19]
	v_lshl_add_u64 v[20:21], s[14:15], 0, v[20:21]
	v_lshl_add_u64 v[20:21], v[20:21], 0, v[16:17]
	v_pk_fma_f32 v[20:21], v[140:141], s[22:23], v[12:13] op_sel_hi:[1,0,1]
	v_pk_fma_f32 v[26:27], v[142:143], s[22:23], v[14:15] op_sel_hi:[1,0,1]
	v_min_f32_e32 v20, 0x40e00000, v20
	v_min_f32_e32 v21, 0x40e00000, v21
	v_pk_mul_f32 v[22:23], v[20:21], s[24:25] op_sel_hi:[1,0]
	v_min_f32_e32 v26, 0x40e00000, v26
	v_exp_f32_e32 v22, v22
	v_exp_f32_e32 v23, v23
	v_min_f32_e32 v27, 0x40e00000, v27
	v_pk_mul_f32 v[28:29], v[26:27], s[24:25] op_sel_hi:[1,0]
	v_med3_f32 v24, v24, s78, v204
	v_pk_add_f32 v[22:23], v[22:23], 1.0 op_sel_hi:[1,0]
	v_exp_f32_e32 v28, v28
	v_rcp_f32_e32 v22, v22
	v_rcp_f32_e32 v23, v23
	v_exp_f32_e32 v29, v29
	v_med3_f32 v25, v25, s78, v204
	v_pk_fma_f32 v[30:31], v[134:135], s[22:23], v[6:7] op_sel_hi:[1,0,1]
	v_pk_mul_f32 v[20:21], v[20:21], v[22:23]
	v_pk_fma_f32 v[22:23], v[24:25], 4.0, 4.0 op_sel_hi:[1,0,0]
	v_pk_fma_f32 v[24:25], v[138:139], s[22:23], v[10:11] op_sel_hi:[1,0,1]
	v_pk_mul_f32 v[20:21], v[22:23], v[20:21]
	v_pk_add_f32 v[22:23], v[28:29], 1.0 op_sel_hi:[1,0]
	v_med3_f32 v24, v24, s78, v204
	v_rcp_f32_e32 v22, v22
	v_rcp_f32_e32 v23, v23
	v_med3_f32 v25, v25, s78, v204
	v_pk_fma_f32 v[24:25], v[24:25], 4.0, 4.0 op_sel_hi:[1,0,0]
	v_min_f32_e32 v30, 0x40e00000, v30
	v_pk_mul_f32 v[22:23], v[26:27], v[22:23]
	v_min_f32_e32 v31, 0x40e00000, v31
	v_pk_mul_f32 v[22:23], v[24:25], v[22:23]
	v_pk_fma_f32 v[24:25], v[132:133], s[22:23], v[4:5] op_sel_hi:[1,0,1]
	v_pk_fma_f32 v[28:29], v[128:129], s[22:23], v[0:1] op_sel_hi:[1,0,1]
	v_min_f32_e32 v24, 0x40e00000, v24
	v_min_f32_e32 v25, 0x40e00000, v25
	v_pk_mul_f32 v[26:27], v[24:25], s[24:25] op_sel_hi:[1,0]
	v_pk_mul_f32 v[128:129], v[30:31], s[24:25] op_sel_hi:[1,0]
	v_exp_f32_e32 v26, v26
	v_exp_f32_e32 v27, v27
	v_exp_f32_e32 v128, v128
	v_exp_f32_e32 v129, v129
	v_med3_f32 v28, v28, s78, v204
	v_pk_add_f32 v[26:27], v[26:27], 1.0 op_sel_hi:[1,0]
	v_med3_f32 v29, v29, s78, v204
	v_rcp_f32_e32 v26, v26
	v_rcp_f32_e32 v27, v27
	s_mov_b64 s[2:3], -1
	v_pk_mul_f32 v[24:25], v[24:25], v[26:27]
	v_pk_fma_f32 v[26:27], v[28:29], 4.0, 4.0 op_sel_hi:[1,0,0]
	v_pk_fma_f32 v[28:29], v[130:131], s[22:23], v[2:3] op_sel_hi:[1,0,1]
	v_pk_mul_f32 v[24:25], v[26:27], v[24:25]
	v_pk_add_f32 v[26:27], v[128:129], 1.0 op_sel_hi:[1,0]
	v_med3_f32 v28, v28, s78, v204
	v_rcp_f32_e32 v26, v26
	v_rcp_f32_e32 v27, v27
	v_med3_f32 v29, v29, s78, v204
	v_pk_mul_f32 v[26:27], v[30:31], v[26:27]
	v_mov_b32_e32 v247, v165
	v_mov_b32_e32 v246, v165
	v_cvt_pk_fp8_f32 v247, v24, v25
	v_cvt_pk_fp8_f32 v246, v20, v21
	v_pk_fma_f32 v[20:21], v[28:29], 4.0, 4.0 op_sel_hi:[1,0,0]
	v_pk_fma_f32 v[24:25], v[120:121], s[22:23], v[8:9] op_sel_hi:[1,0,1]
	v_pk_mul_f32 v[20:21], v[20:21], v[26:27]
	v_cvt_pk_fp8_f32 v246, v22, v23 op_sel:[0,0,1]
	v_cvt_pk_fp8_f32 v247, v20, v21 op_sel:[0,0,1]
	v_add_u32_e32 v20, 16, v18
	v_ashrrev_i32_e32 v21, 31, v20
	v_lshlrev_b64 v[20:21], 10, v[20:21]
	v_lshl_add_u64 v[20:21], s[14:15], 0, v[20:21]
	v_lshl_add_u64 v[20:21], v[20:21], 0, v[16:17]
	s_nop 1
	v_permlane16_swap_b32_e32 v244, v246
	v_permlane16_swap_b32_e32 v245, v247
	v_lshl_add_u64 v[248:249], v[20:21], 0, v[250:251]
	global_store_dwordx4 v[248:249], v[244:247], off
	s_nop 1
	v_pk_fma_f32 v[20:21], v[124:125], s[22:23], v[12:13] op_sel_hi:[1,0,1]
	v_pk_fma_f32 v[26:27], v[126:127], s[22:23], v[14:15] op_sel_hi:[1,0,1]
	v_min_f32_e32 v20, 0x40e00000, v20
	v_min_f32_e32 v21, 0x40e00000, v21
	v_pk_mul_f32 v[22:23], v[20:21], s[24:25] op_sel_hi:[1,0]
	v_min_f32_e32 v26, 0x40e00000, v26
	v_exp_f32_e32 v22, v22
	v_exp_f32_e32 v23, v23
	v_min_f32_e32 v27, 0x40e00000, v27
	v_pk_mul_f32 v[28:29], v[26:27], s[24:25] op_sel_hi:[1,0]
	v_med3_f32 v24, v24, s78, v204
	v_pk_add_f32 v[22:23], v[22:23], 1.0 op_sel_hi:[1,0]
	v_exp_f32_e32 v28, v28
	v_rcp_f32_e32 v22, v22
	v_rcp_f32_e32 v23, v23
	v_exp_f32_e32 v29, v29
	v_med3_f32 v25, v25, s78, v204
	v_pk_fma_f32 v[30:31], v[118:119], s[22:23], v[6:7] op_sel_hi:[1,0,1]
	v_pk_mul_f32 v[20:21], v[20:21], v[22:23]
	v_pk_fma_f32 v[22:23], v[24:25], 4.0, 4.0 op_sel_hi:[1,0,0]
	v_pk_fma_f32 v[24:25], v[122:123], s[22:23], v[10:11] op_sel_hi:[1,0,1]
	v_pk_mul_f32 v[20:21], v[22:23], v[20:21]
	v_pk_add_f32 v[22:23], v[28:29], 1.0 op_sel_hi:[1,0]
	v_med3_f32 v24, v24, s78, v204
	v_rcp_f32_e32 v22, v22
	v_rcp_f32_e32 v23, v23
	v_med3_f32 v25, v25, s78, v204
	v_pk_fma_f32 v[24:25], v[24:25], 4.0, 4.0 op_sel_hi:[1,0,0]
	v_min_f32_e32 v30, 0x40e00000, v30
	v_pk_mul_f32 v[22:23], v[26:27], v[22:23]
	v_min_f32_e32 v31, 0x40e00000, v31
	v_pk_mul_f32 v[22:23], v[24:25], v[22:23]
	v_pk_fma_f32 v[24:25], v[116:117], s[22:23], v[4:5] op_sel_hi:[1,0,1]
	v_pk_fma_f32 v[28:29], v[112:113], s[22:23], v[0:1] op_sel_hi:[1,0,1]
	v_min_f32_e32 v24, 0x40e00000, v24
	v_min_f32_e32 v25, 0x40e00000, v25
	v_pk_mul_f32 v[26:27], v[24:25], s[24:25] op_sel_hi:[1,0]
	v_pk_mul_f32 v[112:113], v[30:31], s[24:25] op_sel_hi:[1,0]
	v_exp_f32_e32 v26, v26
	v_exp_f32_e32 v27, v27
	v_exp_f32_e32 v112, v112
	v_exp_f32_e32 v113, v113
	v_med3_f32 v28, v28, s78, v204
	v_pk_add_f32 v[26:27], v[26:27], 1.0 op_sel_hi:[1,0]
	v_med3_f32 v29, v29, s78, v204
	v_rcp_f32_e32 v26, v26
	v_rcp_f32_e32 v27, v27
	s_nop 0
	v_pk_mul_f32 v[24:25], v[24:25], v[26:27]
	v_pk_fma_f32 v[26:27], v[28:29], 4.0, 4.0 op_sel_hi:[1,0,0]
	v_pk_fma_f32 v[28:29], v[114:115], s[22:23], v[2:3] op_sel_hi:[1,0,1]
	v_pk_mul_f32 v[24:25], v[26:27], v[24:25]
	v_pk_add_f32 v[26:27], v[112:113], 1.0 op_sel_hi:[1,0]
	v_med3_f32 v28, v28, s78, v204
	v_rcp_f32_e32 v26, v26
	v_rcp_f32_e32 v27, v27
	v_med3_f32 v29, v29, s78, v204
	v_pk_mul_f32 v[26:27], v[30:31], v[26:27]
	v_mov_b32_e32 v245, v165
	v_mov_b32_e32 v244, v165
	v_cvt_pk_fp8_f32 v245, v24, v25
	v_cvt_pk_fp8_f32 v244, v20, v21
	v_pk_fma_f32 v[20:21], v[28:29], 4.0, 4.0 op_sel_hi:[1,0,0]
	v_pk_fma_f32 v[24:25], v[104:105], s[22:23], v[8:9] op_sel_hi:[1,0,1]
	v_pk_mul_f32 v[20:21], v[20:21], v[26:27]
	v_cvt_pk_fp8_f32 v244, v22, v23 op_sel:[0,0,1]
	v_cvt_pk_fp8_f32 v245, v20, v21 op_sel:[0,0,1]
	v_add_u32_e32 v20, 32, v18
	v_ashrrev_i32_e32 v21, 31, v20
	v_lshlrev_b64 v[20:21], 10, v[20:21]
	v_lshl_add_u64 v[20:21], s[14:15], 0, v[20:21]
	v_lshl_add_u64 v[20:21], v[20:21], 0, v[16:17]
	v_pk_fma_f32 v[20:21], v[108:109], s[22:23], v[12:13] op_sel_hi:[1,0,1]
	v_pk_fma_f32 v[26:27], v[110:111], s[22:23], v[14:15] op_sel_hi:[1,0,1]
	v_min_f32_e32 v20, 0x40e00000, v20
	v_min_f32_e32 v21, 0x40e00000, v21
	v_pk_mul_f32 v[22:23], v[20:21], s[24:25] op_sel_hi:[1,0]
	v_min_f32_e32 v26, 0x40e00000, v26
	v_exp_f32_e32 v22, v22
	v_exp_f32_e32 v23, v23
	v_min_f32_e32 v27, 0x40e00000, v27
	v_pk_mul_f32 v[28:29], v[26:27], s[24:25] op_sel_hi:[1,0]
	v_med3_f32 v24, v24, s78, v204
	v_pk_add_f32 v[22:23], v[22:23], 1.0 op_sel_hi:[1,0]
	v_exp_f32_e32 v28, v28
	v_rcp_f32_e32 v22, v22
	v_rcp_f32_e32 v23, v23
	v_exp_f32_e32 v29, v29
	v_med3_f32 v25, v25, s78, v204
	v_pk_fma_f32 v[30:31], v[102:103], s[22:23], v[6:7] op_sel_hi:[1,0,1]
	v_pk_mul_f32 v[20:21], v[20:21], v[22:23]
	v_pk_fma_f32 v[22:23], v[24:25], 4.0, 4.0 op_sel_hi:[1,0,0]
	v_pk_fma_f32 v[24:25], v[106:107], s[22:23], v[10:11] op_sel_hi:[1,0,1]
	v_pk_mul_f32 v[20:21], v[22:23], v[20:21]
	v_pk_add_f32 v[22:23], v[28:29], 1.0 op_sel_hi:[1,0]
	v_med3_f32 v24, v24, s78, v204
	v_rcp_f32_e32 v22, v22
	v_rcp_f32_e32 v23, v23
	v_med3_f32 v25, v25, s78, v204
	v_pk_fma_f32 v[24:25], v[24:25], 4.0, 4.0 op_sel_hi:[1,0,0]
	v_min_f32_e32 v30, 0x40e00000, v30
	v_pk_mul_f32 v[22:23], v[26:27], v[22:23]
	v_min_f32_e32 v31, 0x40e00000, v31
	v_pk_mul_f32 v[22:23], v[24:25], v[22:23]
	v_pk_fma_f32 v[24:25], v[100:101], s[22:23], v[4:5] op_sel_hi:[1,0,1]
	v_pk_fma_f32 v[28:29], v[96:97], s[22:23], v[0:1] op_sel_hi:[1,0,1]
	v_min_f32_e32 v24, 0x40e00000, v24
	v_min_f32_e32 v25, 0x40e00000, v25
	v_pk_mul_f32 v[26:27], v[24:25], s[24:25] op_sel_hi:[1,0]
	v_pk_mul_f32 v[96:97], v[30:31], s[24:25] op_sel_hi:[1,0]
	v_exp_f32_e32 v26, v26
	v_exp_f32_e32 v27, v27
	v_exp_f32_e32 v96, v96
	v_exp_f32_e32 v97, v97
	v_med3_f32 v28, v28, s78, v204
	v_pk_add_f32 v[26:27], v[26:27], 1.0 op_sel_hi:[1,0]
	v_med3_f32 v29, v29, s78, v204
	v_rcp_f32_e32 v26, v26
	v_rcp_f32_e32 v27, v27
	s_nop 0
	v_pk_mul_f32 v[24:25], v[24:25], v[26:27]
	v_pk_fma_f32 v[26:27], v[28:29], 4.0, 4.0 op_sel_hi:[1,0,0]
	v_pk_fma_f32 v[28:29], v[98:99], s[22:23], v[2:3] op_sel_hi:[1,0,1]
	v_pk_mul_f32 v[24:25], v[26:27], v[24:25]
	v_pk_add_f32 v[26:27], v[96:97], 1.0 op_sel_hi:[1,0]
	v_med3_f32 v28, v28, s78, v204
	v_rcp_f32_e32 v26, v26
	v_rcp_f32_e32 v27, v27
	v_med3_f32 v29, v29, s78, v204
	v_pk_mul_f32 v[26:27], v[30:31], v[26:27]
	v_mov_b32_e32 v246, v165
	v_cvt_pk_fp8_f32 v246, v20, v21
	v_mov_b32_e32 v247, v165
	v_cvt_pk_fp8_f32 v247, v24, v25
	v_pk_fma_f32 v[20:21], v[28:29], 4.0, 4.0 op_sel_hi:[1,0,0]
	v_cvt_pk_fp8_f32 v246, v22, v23 op_sel:[0,0,1]
	v_pk_fma_f32 v[22:23], v[92:93], s[22:23], v[12:13] op_sel_hi:[1,0,1]
	v_pk_mul_f32 v[20:21], v[20:21], v[26:27]
	v_min_f32_e32 v22, 0x40e00000, v22
	v_min_f32_e32 v23, 0x40e00000, v23
	v_pk_mul_f32 v[24:25], v[22:23], s[24:25] op_sel_hi:[1,0]
	v_cvt_pk_fp8_f32 v247, v20, v21 op_sel:[0,0,1]
	v_add_u32_e32 v20, 48, v18
	v_exp_f32_e32 v24, v24
	v_exp_f32_e32 v25, v25
	v_ashrrev_i32_e32 v21, 31, v20
	v_lshlrev_b64 v[20:21], 10, v[20:21]
	v_lshl_add_u64 v[20:21], s[14:15], 0, v[20:21]
	v_pk_fma_f32 v[28:29], v[94:95], s[22:23], v[14:15] op_sel_hi:[1,0,1]
	v_lshl_add_u64 v[20:21], v[20:21], 0, v[16:17]
	v_pk_add_f32 v[24:25], v[24:25], 1.0 op_sel_hi:[1,0]
	v_min_f32_e32 v28, 0x40e00000, v28
	v_min_f32_e32 v29, 0x40e00000, v29
	s_nop 1
	v_permlane16_swap_b32_e32 v244, v246
	v_permlane16_swap_b32_e32 v245, v247
	v_lshl_add_u64 v[248:249], v[20:21], 0, v[250:251]
	global_store_dwordx4 v[248:249], v[244:247], off
	s_nop 1
	v_rcp_f32_e32 v24, v24
	v_rcp_f32_e32 v25, v25
	v_pk_mul_f32 v[30:31], v[28:29], s[24:25] op_sel_hi:[1,0]
	v_pk_fma_f32 v[26:27], v[88:89], s[22:23], v[8:9] op_sel_hi:[1,0,1]
	v_exp_f32_e32 v30, v30
	v_exp_f32_e32 v31, v31
	v_med3_f32 v26, v26, s78, v204
	v_med3_f32 v27, v27, s78, v204
	v_pk_mul_f32 v[22:23], v[22:23], v[24:25]
	v_pk_fma_f32 v[24:25], v[26:27], 4.0, 4.0 op_sel_hi:[1,0,0]
	v_pk_fma_f32 v[26:27], v[90:91], s[22:23], v[10:11] op_sel_hi:[1,0,1]
	v_pk_mul_f32 v[22:23], v[24:25], v[22:23]
	v_pk_add_f32 v[24:25], v[30:31], 1.0 op_sel_hi:[1,0]
	v_med3_f32 v26, v26, s78, v204
	v_rcp_f32_e32 v24, v24
	v_rcp_f32_e32 v25, v25
	v_med3_f32 v27, v27, s78, v204
	v_pk_fma_f32 v[26:27], v[26:27], 4.0, 4.0 op_sel_hi:[1,0,0]
	v_pk_fma_f32 v[30:31], v[80:81], s[22:23], v[0:1] op_sel_hi:[1,0,1]
	v_pk_mul_f32 v[24:25], v[28:29], v[24:25]
	v_pk_fma_f32 v[80:81], v[86:87], s[22:23], v[6:7] op_sel_hi:[1,0,1]
	v_pk_mul_f32 v[24:25], v[26:27], v[24:25]
	v_pk_fma_f32 v[26:27], v[84:85], s[22:23], v[4:5] op_sel_hi:[1,0,1]
	v_min_f32_e32 v80, 0x40e00000, v80
	v_min_f32_e32 v26, 0x40e00000, v26
	v_min_f32_e32 v27, 0x40e00000, v27
	v_pk_mul_f32 v[28:29], v[26:27], s[24:25] op_sel_hi:[1,0]
	v_min_f32_e32 v81, 0x40e00000, v81
	v_exp_f32_e32 v28, v28
	v_exp_f32_e32 v29, v29
	v_pk_mul_f32 v[84:85], v[80:81], s[24:25] op_sel_hi:[1,0]
	v_med3_f32 v30, v30, s78, v204
	v_exp_f32_e32 v84, v84
	v_pk_add_f32 v[28:29], v[28:29], 1.0 op_sel_hi:[1,0]
	v_exp_f32_e32 v85, v85
	v_rcp_f32_e32 v28, v28
	v_rcp_f32_e32 v29, v29
	v_med3_f32 v31, v31, s78, v204
	v_add_u32_e32 v20, 0x80, v18
	v_ashrrev_i32_e32 v21, 31, v20
	v_pk_mul_f32 v[26:27], v[26:27], v[28:29]
	v_pk_fma_f32 v[28:29], v[30:31], 4.0, 4.0 op_sel_hi:[1,0,0]
	v_pk_fma_f32 v[30:31], v[82:83], s[22:23], v[2:3] op_sel_hi:[1,0,1]
	v_pk_mul_f32 v[26:27], v[28:29], v[26:27]
	v_pk_add_f32 v[28:29], v[84:85], 1.0 op_sel_hi:[1,0]
	v_med3_f32 v30, v30, s78, v204
	v_rcp_f32_e32 v28, v28
	v_rcp_f32_e32 v29, v29
	v_med3_f32 v31, v31, s78, v204
	v_lshlrev_b64 v[20:21], 10, v[20:21]
	v_lshl_add_u64 v[20:21], s[14:15], 0, v[20:21]
	v_pk_mul_f32 v[28:29], v[80:81], v[28:29]
	v_mov_b32_e32 v244, v165
	v_mov_b32_e32 v245, v165
	v_cvt_pk_fp8_f32 v244, v22, v23
	v_cvt_pk_fp8_f32 v245, v26, v27
	v_pk_fma_f32 v[22:23], v[30:31], 4.0, 4.0 op_sel_hi:[1,0,0]
	v_lshl_add_u64 v[20:21], v[20:21], 0, v[16:17]
	v_pk_mul_f32 v[22:23], v[22:23], v[28:29]
	v_cvt_pk_fp8_f32 v244, v24, v25 op_sel:[0,0,1]
	v_cvt_pk_fp8_f32 v245, v22, v23 op_sel:[0,0,1]
	v_pk_fma_f32 v[26:27], v[78:79], s[22:23], v[14:15] op_sel_hi:[1,0,1]
	v_pk_fma_f32 v[24:25], v[72:73], s[22:23], v[8:9] op_sel_hi:[1,0,1]
	v_min_f32_e32 v26, 0x40e00000, v26
	v_pk_fma_f32 v[20:21], v[76:77], s[22:23], v[12:13] op_sel_hi:[1,0,1]
	v_min_f32_e32 v27, 0x40e00000, v27
	v_min_f32_e32 v20, 0x40e00000, v20
	v_min_f32_e32 v21, 0x40e00000, v21
	v_pk_mul_f32 v[22:23], v[20:21], s[24:25] op_sel_hi:[1,0]
	v_pk_mul_f32 v[28:29], v[26:27], s[24:25] op_sel_hi:[1,0]
	v_exp_f32_e32 v22, v22
	v_exp_f32_e32 v23, v23
	v_exp_f32_e32 v28, v28
	v_exp_f32_e32 v29, v29
	v_med3_f32 v24, v24, s78, v204
	v_pk_add_f32 v[22:23], v[22:23], 1.0 op_sel_hi:[1,0]
	v_med3_f32 v25, v25, s78, v204
	v_rcp_f32_e32 v22, v22
	v_rcp_f32_e32 v23, v23
	v_pk_fma_f32 v[30:31], v[70:71], s[22:23], v[6:7] op_sel_hi:[1,0,1]
	v_pk_mul_f32 v[20:21], v[20:21], v[22:23]
	v_pk_fma_f32 v[22:23], v[24:25], 4.0, 4.0 op_sel_hi:[1,0,0]
	v_pk_fma_f32 v[24:25], v[74:75], s[22:23], v[10:11] op_sel_hi:[1,0,1]
	v_pk_mul_f32 v[20:21], v[22:23], v[20:21]
	v_pk_add_f32 v[22:23], v[28:29], 1.0 op_sel_hi:[1,0]
	v_med3_f32 v24, v24, s78, v204
	v_rcp_f32_e32 v22, v22
	v_rcp_f32_e32 v23, v23
	v_med3_f32 v25, v25, s78, v204
	v_pk_fma_f32 v[24:25], v[24:25], 4.0, 4.0 op_sel_hi:[1,0,0]
	v_min_f32_e32 v30, 0x40e00000, v30
	v_pk_mul_f32 v[22:23], v[26:27], v[22:23]
	v_min_f32_e32 v31, 0x40e00000, v31
	v_pk_mul_f32 v[22:23], v[24:25], v[22:23]
	v_pk_fma_f32 v[24:25], v[68:69], s[22:23], v[4:5] op_sel_hi:[1,0,1]
	v_pk_fma_f32 v[28:29], v[64:65], s[22:23], v[0:1] op_sel_hi:[1,0,1]
	v_min_f32_e32 v24, 0x40e00000, v24
	v_min_f32_e32 v25, 0x40e00000, v25
	v_pk_mul_f32 v[26:27], v[24:25], s[24:25] op_sel_hi:[1,0]
	v_pk_mul_f32 v[64:65], v[30:31], s[24:25] op_sel_hi:[1,0]
	v_exp_f32_e32 v26, v26
	v_exp_f32_e32 v27, v27
	v_exp_f32_e32 v64, v64
	v_exp_f32_e32 v65, v65
	v_med3_f32 v28, v28, s78, v204
	v_pk_add_f32 v[26:27], v[26:27], 1.0 op_sel_hi:[1,0]
	v_med3_f32 v29, v29, s78, v204
	v_rcp_f32_e32 v26, v26
	v_rcp_f32_e32 v27, v27
	s_nop 0
	v_pk_mul_f32 v[24:25], v[24:25], v[26:27]
	v_pk_fma_f32 v[26:27], v[28:29], 4.0, 4.0 op_sel_hi:[1,0,0]
	v_pk_fma_f32 v[28:29], v[66:67], s[22:23], v[2:3] op_sel_hi:[1,0,1]
	v_pk_mul_f32 v[24:25], v[26:27], v[24:25]
	v_pk_add_f32 v[26:27], v[64:65], 1.0 op_sel_hi:[1,0]
	v_med3_f32 v28, v28, s78, v204
	v_rcp_f32_e32 v26, v26
	v_rcp_f32_e32 v27, v27
	v_med3_f32 v29, v29, s78, v204
	v_pk_mul_f32 v[26:27], v[30:31], v[26:27]
	v_mov_b32_e32 v247, v165
	v_mov_b32_e32 v246, v165
	v_cvt_pk_fp8_f32 v247, v24, v25
	v_cvt_pk_fp8_f32 v246, v20, v21
	v_pk_fma_f32 v[20:21], v[28:29], 4.0, 4.0 op_sel_hi:[1,0,0]
	v_pk_fma_f32 v[24:25], v[56:57], s[22:23], v[8:9] op_sel_hi:[1,0,1]
	v_pk_mul_f32 v[20:21], v[20:21], v[26:27]
	v_cvt_pk_fp8_f32 v246, v22, v23 op_sel:[0,0,1]
	v_cvt_pk_fp8_f32 v247, v20, v21 op_sel:[0,0,1]
	v_add_u32_e32 v20, 0x90, v18
	v_ashrrev_i32_e32 v21, 31, v20
	v_lshlrev_b64 v[20:21], 10, v[20:21]
	v_lshl_add_u64 v[20:21], s[14:15], 0, v[20:21]
	v_lshl_add_u64 v[20:21], v[20:21], 0, v[16:17]
	s_nop 1
	v_permlane16_swap_b32_e32 v244, v246
	v_permlane16_swap_b32_e32 v245, v247
	v_lshl_add_u64 v[248:249], v[20:21], 0, v[250:251]
	global_store_dwordx4 v[248:249], v[244:247], off
	s_nop 1
	v_pk_fma_f32 v[20:21], v[60:61], s[22:23], v[12:13] op_sel_hi:[1,0,1]
	v_pk_fma_f32 v[26:27], v[62:63], s[22:23], v[14:15] op_sel_hi:[1,0,1]
	v_min_f32_e32 v20, 0x40e00000, v20
	v_min_f32_e32 v21, 0x40e00000, v21
	v_pk_mul_f32 v[22:23], v[20:21], s[24:25] op_sel_hi:[1,0]
	v_min_f32_e32 v26, 0x40e00000, v26
	v_exp_f32_e32 v22, v22
	v_exp_f32_e32 v23, v23
	v_min_f32_e32 v27, 0x40e00000, v27
	v_pk_mul_f32 v[28:29], v[26:27], s[24:25] op_sel_hi:[1,0]
	v_med3_f32 v24, v24, s78, v204
	v_pk_add_f32 v[22:23], v[22:23], 1.0 op_sel_hi:[1,0]
	v_exp_f32_e32 v28, v28
	v_rcp_f32_e32 v22, v22
	v_rcp_f32_e32 v23, v23
	v_exp_f32_e32 v29, v29
	v_med3_f32 v25, v25, s78, v204
	v_pk_fma_f32 v[30:31], v[54:55], s[22:23], v[6:7] op_sel_hi:[1,0,1]
	v_pk_mul_f32 v[20:21], v[20:21], v[22:23]
	v_pk_fma_f32 v[22:23], v[24:25], 4.0, 4.0 op_sel_hi:[1,0,0]
	v_pk_fma_f32 v[24:25], v[58:59], s[22:23], v[10:11] op_sel_hi:[1,0,1]
	v_pk_mul_f32 v[20:21], v[22:23], v[20:21]
	v_pk_add_f32 v[22:23], v[28:29], 1.0 op_sel_hi:[1,0]
	v_med3_f32 v24, v24, s78, v204
	v_rcp_f32_e32 v22, v22
	v_rcp_f32_e32 v23, v23
	v_med3_f32 v25, v25, s78, v204
	v_pk_fma_f32 v[24:25], v[24:25], 4.0, 4.0 op_sel_hi:[1,0,0]
	v_min_f32_e32 v30, 0x40e00000, v30
	v_pk_mul_f32 v[22:23], v[26:27], v[22:23]
	v_min_f32_e32 v31, 0x40e00000, v31
	v_pk_mul_f32 v[22:23], v[24:25], v[22:23]
	v_pk_fma_f32 v[24:25], v[52:53], s[22:23], v[4:5] op_sel_hi:[1,0,1]
	v_pk_fma_f32 v[28:29], v[48:49], s[22:23], v[0:1] op_sel_hi:[1,0,1]
	v_min_f32_e32 v24, 0x40e00000, v24
	v_min_f32_e32 v25, 0x40e00000, v25
	v_pk_mul_f32 v[26:27], v[24:25], s[24:25] op_sel_hi:[1,0]
	v_pk_mul_f32 v[48:49], v[30:31], s[24:25] op_sel_hi:[1,0]
	v_exp_f32_e32 v26, v26
	v_exp_f32_e32 v27, v27
	v_exp_f32_e32 v48, v48
	v_exp_f32_e32 v49, v49
	v_med3_f32 v28, v28, s78, v204
	v_pk_add_f32 v[26:27], v[26:27], 1.0 op_sel_hi:[1,0]
	v_med3_f32 v29, v29, s78, v204
	v_rcp_f32_e32 v26, v26
	v_rcp_f32_e32 v27, v27
	v_pk_fma_f32 v[12:13], v[44:45], s[22:23], v[12:13] op_sel_hi:[1,0,1]
	v_pk_fma_f32 v[14:15], v[46:47], s[22:23], v[14:15] op_sel_hi:[1,0,1]
	v_min_f32_e32 v12, 0x40e00000, v12
	v_pk_mul_f32 v[24:25], v[24:25], v[26:27]
	v_pk_fma_f32 v[26:27], v[28:29], 4.0, 4.0 op_sel_hi:[1,0,0]
	v_pk_fma_f32 v[28:29], v[50:51], s[22:23], v[2:3] op_sel_hi:[1,0,1]
	v_pk_mul_f32 v[24:25], v[26:27], v[24:25]
	v_pk_add_f32 v[26:27], v[48:49], 1.0 op_sel_hi:[1,0]
	v_med3_f32 v28, v28, s78, v204
	v_rcp_f32_e32 v26, v26
	v_rcp_f32_e32 v27, v27
	v_med3_f32 v29, v29, s78, v204
	v_min_f32_e32 v13, 0x40e00000, v13
	v_min_f32_e32 v14, 0x40e00000, v14
	v_pk_mul_f32 v[26:27], v[30:31], v[26:27]
	v_mov_b32_e32 v245, v165
	v_mov_b32_e32 v244, v165
	v_cvt_pk_fp8_f32 v245, v24, v25
	v_cvt_pk_fp8_f32 v244, v20, v21
	v_pk_fma_f32 v[20:21], v[28:29], 4.0, 4.0 op_sel_hi:[1,0,0]
	v_min_f32_e32 v15, 0x40e00000, v15
	v_pk_mul_f32 v[20:21], v[20:21], v[26:27]
	v_cvt_pk_fp8_f32 v244, v22, v23 op_sel:[0,0,1]
	v_cvt_pk_fp8_f32 v245, v20, v21 op_sel:[0,0,1]
	v_add_u32_e32 v20, 0xa0, v18
	v_ashrrev_i32_e32 v21, 31, v20
	v_lshlrev_b64 v[20:21], 10, v[20:21]
	v_lshl_add_u64 v[20:21], s[14:15], 0, v[20:21]
	v_lshl_add_u64 v[20:21], v[20:21], 0, v[16:17]
	v_pk_mul_f32 v[20:21], v[12:13], s[24:25] op_sel_hi:[1,0]
	v_pk_mul_f32 v[22:23], v[14:15], s[24:25] op_sel_hi:[1,0]
	v_exp_f32_e32 v20, v20
	v_exp_f32_e32 v21, v21
	v_exp_f32_e32 v22, v22
	v_exp_f32_e32 v23, v23
	v_pk_fma_f32 v[8:9], v[40:41], s[22:23], v[8:9] op_sel_hi:[1,0,1]
	v_pk_add_f32 v[20:21], v[20:21], 1.0 op_sel_hi:[1,0]
	v_med3_f32 v8, v8, s78, v204
	v_rcp_f32_e32 v20, v20
	v_rcp_f32_e32 v21, v21
	v_med3_f32 v9, v9, s78, v204
	v_pk_fma_f32 v[8:9], v[8:9], 4.0, 4.0 op_sel_hi:[1,0,0]
	v_pk_fma_f32 v[10:11], v[42:43], s[22:23], v[10:11] op_sel_hi:[1,0,1]
	v_pk_mul_f32 v[12:13], v[12:13], v[20:21]
	v_med3_f32 v10, v10, s78, v204
	v_pk_mul_f32 v[8:9], v[8:9], v[12:13]
	v_pk_add_f32 v[12:13], v[22:23], 1.0 op_sel_hi:[1,0]
	v_med3_f32 v11, v11, s78, v204
	v_rcp_f32_e32 v12, v12
	v_rcp_f32_e32 v13, v13
	v_pk_fma_f32 v[4:5], v[36:37], s[22:23], v[4:5] op_sel_hi:[1,0,1]
	v_pk_fma_f32 v[10:11], v[10:11], 4.0, 4.0 op_sel_hi:[1,0,0]
	v_min_f32_e32 v4, 0x40e00000, v4
	v_pk_mul_f32 v[12:13], v[14:15], v[12:13]
	v_min_f32_e32 v5, 0x40e00000, v5
	v_pk_mul_f32 v[10:11], v[10:11], v[12:13]
	v_pk_mul_f32 v[12:13], v[4:5], s[24:25] op_sel_hi:[1,0]
	v_pk_fma_f32 v[6:7], v[38:39], s[22:23], v[6:7] op_sel_hi:[1,0,1]
	v_exp_f32_e32 v12, v12
	v_exp_f32_e32 v13, v13
	v_min_f32_e32 v6, 0x40e00000, v6
	v_min_f32_e32 v7, 0x40e00000, v7
	v_pk_mul_f32 v[14:15], v[6:7], s[24:25] op_sel_hi:[1,0]
	v_pk_add_f32 v[12:13], v[12:13], 1.0 op_sel_hi:[1,0]
	v_exp_f32_e32 v14, v14
	v_rcp_f32_e32 v12, v12
	v_rcp_f32_e32 v13, v13
	v_exp_f32_e32 v15, v15
	v_pk_fma_f32 v[0:1], v[32:33], s[22:23], v[0:1] op_sel_hi:[1,0,1]
	v_pk_fma_f32 v[2:3], v[34:35], s[22:23], v[2:3] op_sel_hi:[1,0,1]
	v_med3_f32 v0, v0, s78, v204
	v_med3_f32 v1, v1, s78, v204
	v_pk_mul_f32 v[4:5], v[4:5], v[12:13]
	v_pk_fma_f32 v[0:1], v[0:1], 4.0, 4.0 op_sel_hi:[1,0,0]
	v_med3_f32 v2, v2, s78, v204
	v_pk_mul_f32 v[0:1], v[0:1], v[4:5]
	v_pk_add_f32 v[4:5], v[14:15], 1.0 op_sel_hi:[1,0]
	v_med3_f32 v3, v3, s78, v204
	v_rcp_f32_e32 v4, v4
	v_rcp_f32_e32 v5, v5
	s_nop 0
	v_pk_mul_f32 v[4:5], v[6:7], v[4:5]
	v_mov_b32_e32 v247, v165
	v_mov_b32_e32 v246, v165
	v_cvt_pk_fp8_f32 v247, v0, v1
	v_cvt_pk_fp8_f32 v246, v8, v9
	v_pk_fma_f32 v[0:1], v[2:3], 4.0, 4.0 op_sel_hi:[1,0,0]
	v_cvt_pk_fp8_f32 v246, v10, v11 op_sel:[0,0,1]
	v_pk_mul_f32 v[0:1], v[0:1], v[4:5]
	s_nop 0
	v_cvt_pk_fp8_f32 v247, v0, v1 op_sel:[0,0,1]
	v_add_u32_e32 v0, 0xb0, v18
	v_ashrrev_i32_e32 v1, 31, v0
	v_lshlrev_b64 v[0:1], 10, v[0:1]
	v_lshl_add_u64 v[0:1], s[14:15], 0, v[0:1]
	v_lshl_add_u64 v[0:1], v[0:1], 0, v[16:17]
	s_nop 1
	v_permlane16_swap_b32_e32 v244, v246
	v_permlane16_swap_b32_e32 v245, v247
	v_lshl_add_u64 v[248:249], v[0:1], 0, v[250:251]
	global_store_dwordx4 v[248:249], v[244:247], off
	s_nop 1
	s_cbranch_vccnz .LBB0_1700
	s_andn2_b64 vcc, exec, s[12:13]
	s_cbranch_vccnz .LBB0_1699
	s_barrier
	s_branch .LBB0_1699
